# variant: P7 unit permutation 2 blocks x 16 column tiles per XCD (was 4 x 8)
# speedup vs baseline: 1.0022x; 1.0022x over previous
; #define LAS __attribute__((address_space(3)))
; template <class Epi, class Sched, bool GATHER, bool FP8>
; __device__ __forceinline__ void gemm_phase(LAS uchar* lds, const int K, const int LDA, const int LDB, const size_t kstepA, const size_t kstepB, const Sched& S, const Epi& E) {
;     ...
;     Unit cur, nxt; int ui = 0;
;     if (!S.next(0, cur)) return;
;     f32x4 acc[2][2][4][2];
; #pragma unroll
;     for (int a = 0; a < 2; ++a)
; #pragma unroll
;         for (int b = 0; b < 2; ++b)
; #pragma unroll
;             for (int m = 0; m < 4; ++m)
; #pragma unroll
;                 for (int n = 0; n < 2; ++n) acc[a][b][m][n] = (f32x4){0.f, 0.f, 0.f, 0.f};
;     bf16x8 At[4][2], B0[2][2], B1[2][2];
;     const char* cA = cur.pa; const char* cB = cur.pb;
;     if constexpr (GATHER) S.gather(cur, voA, (const LAS int*)nullptr);
;     __device__ __forceinline__ bool next(int i, pg8::Unit& u) const {
;         const int NB = __builtin_amdgcn_readfirstlane(tab[0]); const int L = i * G + c; if (L >= NB * nN) return false;
;         const int b = L / nN, pn = L - b * nN, e = __builtin_amdgcn_readfirstlane(tab[64 + b]);
;         u.pa = A; u.pb = B + (size_t)e * bexp + (size_t)pn * 256 * 128; u.row0 = b * 256; u.col0 = pn * 256; u.aux = e; u.blk = b; return true;
;     }
;     __device__ __forceinline__ void prefetch(const pg8::Unit& u, LAS uchar* buf, int wid, int lane) const {
;         { const int e = u.aux, lb = (u.blk - __builtin_amdgcn_readfirstlane(tab[8 + e])) * 256, w4 = wid & 3;
;             __builtin_amdgcn_global_load_lds((const unsigned*)(list + e * T + lb + 64 * w4 + lane), (LAS unsigned*)(buf + w4 * 256), 4, 0, 0); }
;     }
;     __device__ __forceinline__ void gather(const pg8::Unit& u, unsigned (&vo)[2][2], const LAS int* idx) const {
;         const int e = u.aux, lb = (u.blk - __builtin_amdgcn_readfirstlane(tab[8 + e])) * 256, cnt = __builtin_amdgcn_readfirstlane(tab[256 + u.blk]);
; #pragma unroll
;         for (int i = 0; i < 2; ++i) { int R, C; pg8::stage_rc((int)threadIdx.x * 16 + i * 8192, R, C);
; #pragma unroll
;             for (int h = 0; h < 2; ++h) { const int r = h * 128 + R; const int raw = idx ? idx[r] : list[e * T + lb + r]; const int tok = (r < cnt) ? raw : 0; vo[h][i] = ((unsigned)tok * (unsigned)K + (unsigned)C) * 2u; } }
;     }
.LBB0_917:
	s_or_b64 exec, exec, s[8:9]
	s_add_i32 s12, 0, 0x22000
	s_waitcnt vmcnt(4)
	v_mov_b32_e32 v2, s12
	s_waitcnt lgkmcnt(0)
	s_barrier
	ds_read_b32 v2, v2
	v_readfirstlane_b32 s20, v0
	s_waitcnt lgkmcnt(0)
	v_readfirstlane_b32 s2, v2
	s_lshl_b32 s2, s2, 4
	s_and_b32 s98, s87, 7
	s_lshl_b32 s98, s98, 5
	s_lshr_b32 s99, s87, 3
	s_or_b32 s98, s98, s99
	s_cmpk_eq_i32 s92, 0x100
	s_cselect_b32 s98, s98, s87
	s_cmp_ge_i32 s98, s2
	s_cbranch_scc1 .LBB0_937
	s_add_u32 s8, s90, 0x6000000
	s_addc_u32 s9, s91, 0
	s_add_u32 s25, s90, 0x30000000
	s_addc_u32 s33, s91, 0
	s_add_u32 s10, s90, 0x2f00000
	s_addc_u32 s11, s91, 0
	s_ashr_i32 s2, s98, 31
	s_lshr_b32 s2, s2, 28
	s_add_i32 s2, s98, s2
	s_ashr_i32 s18, s2, 4
	s_lshl_b32 s3, s18, 2
	s_add_i32 s3, s12, s3
	v_mov_b32_e32 v2, s3
	ds_read2st64_b32 v[2:3], v2 offset0:1 offset1:4
	s_lshr_b32 s21, s20, 6
	s_and_b32 s2, s2, -16
	s_lshr_b32 s22, s20, 8
	s_lshl_b32 s52, s21, 10
	s_waitcnt lgkmcnt(0)
	v_readfirstlane_b32 s42, v2
	s_ashr_i32 s43, s42, 31
	s_sub_i32 s2, s98, s2
	s_lshl_b64 s[14:15], s[42:43], 23
	s_add_u32 s13, s25, s14
	s_addc_u32 s16, s33, s15
	s_ashr_i32 s3, s2, 31
	s_lshl_b64 s[14:15], s[2:3], 15
	s_add_u32 s44, s13, s14
	s_addc_u32 s45, s16, s15
	s_lshl_b32 s3, s42, 2
	s_add_i32 s3, s12, s3
	v_mov_b32_e32 v2, s3
	ds_read_b32 v2, v2 offset:32
	v_lshrrev_b32_e32 v13, 3, v0
	v_bfe_u32 v12, v0, 2, 4
	v_or_b32_e32 v4, 64, v13
	s_movk_i32 s3, 0x70
	v_and_or_b32 v195, v4, s3, v12
	s_waitcnt lgkmcnt(0)
	v_readfirstlane_b32 s3, v2
	s_sub_i32 s3, s18, s3
	s_lshl_b32 s3, s3, 8
	s_lshl_b32 s12, s42, 13
	s_add_i32 s3, s3, s12
	v_and_or_b32 v208, v13, 48, v12
	v_or_b32_e32 v4, s3, v208
	v_or_b32_e32 v209, 0x80, v208
	v_or_b32_e32 v210, 0x80, v195
	v_ashrrev_i32_e32 v5, 31, v4
	v_or_b32_e32 v6, s3, v209
	v_or_b32_e32 v8, s3, v195
	v_or_b32_e32 v10, s3, v210
	v_lshl_add_u64 v[4:5], v[4:5], 2, s[10:11]
	v_ashrrev_i32_e32 v7, 31, v6
	v_ashrrev_i32_e32 v9, 31, v8
	v_ashrrev_i32_e32 v11, 31, v10
	v_lshl_add_u64 v[6:7], v[6:7], 2, s[10:11]
	v_lshl_add_u64 v[8:9], v[8:9], 2, s[10:11]
	v_lshl_add_u64 v[10:11], v[10:11], 2, s[10:11]
	global_load_dword v14, v[4:5], off
	global_load_dword v15, v[6:7], off
	global_load_dword v16, v[8:9], off
	global_load_dword v17, v[10:11], off
	v_lshlrev_b32_e32 v4, 4, v0
	v_and_b32_e32 v5, 32, v0
	v_bitop3_b32 v4, v4, v5, 48 bitop3:0x6c
	v_and_or_b32 v5, v13, 32, v12
	v_and_b32_e32 v2, 48, v0
	s_movk_i32 s14, 0x46
	v_and_or_b32 v211, v0, 64, v4
	v_lshlrev_b32_e32 v4, 1, v5
	s_movk_i32 s3, 0xc6
	v_lshlrev_b32_e32 v5, 1, v195
	v_and_or_b32 v4, v4, s14, v2
	s_add_i32 s53, s52, 0
	v_and_b32_e32 v6, 0x80, v0
	v_mov_b32_e32 v197, 0
	v_and_or_b32 v5, v5, s3, v2
	v_lshlrev_b32_e32 v4, 7, v4
	s_add_i32 s54, s53, 0x10000
	v_mov_b32_e32 v199, v197
	v_lshlrev_b32_e32 v5, 7, v5
	v_or3_b32 v198, v4, v6, v211
	s_add_i32 s55, s53, 0x12000
	s_mov_b32 m0, s54
	s_mov_b64 s[12:13], 0x400
	v_or3_b32 v200, v5, v6, v211
	v_readfirstlane_b32 s3, v3
	v_lshl_add_u64 v[4:5], s[44:45], 0, v[198:199]
	s_add_i32 s56, s53, 0x14000
	global_load_lds_dwordx4 v198, s[44:45]
	s_mov_b32 m0, s55
	v_mov_b32_e32 v201, v197
	v_lshl_add_u64 v[4:5], v[4:5], 0, s[12:13]
	global_load_lds_dwordx4 v200, s[44:45]
	s_mov_b32 m0, s56
	v_cmp_gt_i32_e32 vcc, s3, v208
	v_lshl_add_u64 v[6:7], s[44:45], 0, v[200:201]
	s_add_i32 s57, s53, 0x16000
	global_load_lds_dwordx4 v[4:5], off
	v_lshl_add_u64 v[6:7], v[6:7], 0, s[12:13]
	s_mov_b32 m0, s57
	s_add_i32 s58, s53, 0x2000
	global_load_lds_dwordx4 v[6:7], off
	s_mov_b32 m0, s53
	s_add_i32 s59, s53, 0x4000
	s_add_i32 s60, s53, 0x6000
	s_load_dwordx2 s[14:15], s[0:1], 0x78
	s_cmp_eq_u32 s22, 1
	s_mov_b32 s46, 0
	s_cselect_b64 s[16:17], -1, 0
	s_cmp_lg_u32 s22, 1
	v_mov_b32_e32 v203, v197
	s_waitcnt vmcnt(0)
	v_mul_u32_u24_e32 v3, 0x880, v14
	v_mul_u32_u24_e32 v4, 0x880, v15
	v_cndmask_b32_e32 v3, 0, v3, vcc
	v_cmp_gt_i32_e32 vcc, s3, v209
	v_mul_u32_u24_e32 v5, 0x880, v16
	v_or_b32_e32 v196, v3, v211
	v_cndmask_b32_e32 v4, 0, v4, vcc
	v_cmp_gt_i32_e32 vcc, s3, v195
	v_mul_u32_u24_e32 v6, 0x880, v17
	global_load_lds_dwordx4 v196, s[8:9]
	v_cndmask_b32_e32 v5, 0, v5, vcc
	v_cmp_gt_i32_e32 vcc, s3, v210
	v_or_b32_e32 v202, v5, v211
	s_mov_b32 m0, s58
	v_cndmask_b32_e32 v6, 0, v6, vcc
	v_or_b32_e32 v3, v4, v211
	global_load_lds_dwordx4 v202, s[8:9]
	s_mov_b32 m0, s59
	v_or_b32_e32 v204, v6, v211
	global_load_lds_dwordx4 v3, s[8:9]
	s_mov_b32 m0, s60
	s_nop 0
	global_load_lds_dwordx4 v204, s[8:9]
	s_cbranch_scc1 .LBB0_920
	s_barrier
